# speedup vs baseline: 1.0155x; 1.0137x over previous
.LBB3_2:
	v_exp_f32_e32 v81, v112
	v_exp_f32_e32 v82, v113
	v_exp_f32_e32 v85, v116
	v_exp_f32_e32 v86, v117
	v_exp_f32_e32 v89, v120
	v_exp_f32_e32 v90, v121
	v_exp_f32_e32 v93, v124
	v_exp_f32_e32 v94, v125
	v_exp_f32_e32 v64, v64
	v_exp_f32_e32 v65, v65
	v_exp_f32_e32 v68, v68
	v_exp_f32_e32 v69, v69
	v_exp_f32_e32 v72, v72
	v_exp_f32_e32 v73, v73
	v_exp_f32_e32 v76, v76
	v_exp_f32_e32 v77, v77
	v_exp_f32_e32 v83, v114
	v_exp_f32_e32 v84, v115
	v_exp_f32_e32 v87, v118
	v_exp_f32_e32 v88, v119
	v_exp_f32_e32 v91, v122
	v_exp_f32_e32 v92, v123
	v_exp_f32_e32 v95, v126
	v_exp_f32_e32 v96, v127
	v_exp_f32_e32 v66, v66
	v_exp_f32_e32 v67, v67
	v_exp_f32_e32 v70, v70
	v_exp_f32_e32 v71, v71
	v_exp_f32_e32 v74, v74
	v_exp_f32_e32 v75, v75
	v_exp_f32_e32 v78, v78
	v_exp_f32_e32 v79, v79
	v_cvt_pk_fp8_f32 v160, v81, v82
	v_cvt_pk_fp8_f32 v161, v85, v86
	v_cvt_pk_fp8_f32 v162, v89, v90
	v_cvt_pk_fp8_f32 v163, v93, v94
	v_cvt_pk_fp8_f32 v164, v64, v65
	v_cvt_pk_fp8_f32 v165, v68, v69
	v_cvt_pk_fp8_f32 v166, v72, v73
	v_cvt_pk_fp8_f32 v167, v76, v77
	v_cvt_pk_fp8_f32 v160, v83, v84 op_sel:[0,0,1]
	v_cvt_pk_fp8_f32 v161, v87, v88 op_sel:[0,0,1]
	v_cvt_pk_fp8_f32 v162, v91, v92 op_sel:[0,0,1]
	v_cvt_pk_fp8_f32 v163, v95, v96 op_sel:[0,0,1]
	v_cvt_pk_fp8_f32 v164, v66, v67 op_sel:[0,0,1]
	v_cvt_pk_fp8_f32 v165, v70, v71 op_sel:[0,0,1]
	v_cvt_pk_fp8_f32 v166, v74, v75 op_sel:[0,0,1]
	v_cvt_pk_fp8_f32 v167, v78, v79 op_sel:[0,0,1]
	s_lshl_b32 s6, s4, 7
	s_and_b32 s6, s6, 0xfffffc00
	v_mfma_scale_f32_16x16x128_f8f6f4 v[48:51], v[144:151], v[160:167], v[48:51], v194, v194 op_sel_hi:[0,0,0]
	s_nop 15
	s_nop 3
	s_lshl_b32 s4, s4, 6
	v_mul_f32_e32 v48, 0x41800000, v48
	s_waitcnt lgkmcnt(0)
	v_mfma_scale_f32_32x32x64_f8f6f4 v[32:47], v[128:135], v[160:167], v[32:47], v194, v194 op_sel_hi:[0,0,0]
	v_div_scale_f32 v49, s[30:31], v48, v48, s37
	v_rcp_f32_e32 v66, v49
	s_mov_b64 s[30:31], 0
	v_fma_f32 v50, -v49, v66, 1.0
	v_fmac_f32_e32 v66, v50, v66
	v_div_scale_f32 v50, vcc, s37, v48, s37
	v_mul_f32_e32 v51, v50, v66
	v_fma_f32 v52, -v49, v51, v50
	v_fmac_f32_e32 v51, v52, v66
	v_fma_f32 v49, -v49, v51, v50
	v_div_fmas_f32 v49, v49, v66, v51
	v_mfma_scale_f32_32x32x64_f8f6f4 v[16:31], v[136:143], v[160:167], v[16:31], v194, v194 op_sel_hi:[0,0,0]
	v_div_fixup_f32 v48, v49, v48, s37
	s_nop 6
	v_mul_f32_e32 v32, v48, v32
	v_mul_f32_e32 v33, v48, v33
	v_mov_b32_e32 v49, 0
	v_cvt_pk_fp8_f32 v49, v32, v33
	v_mul_f32_e32 v32, v48, v34
	v_mul_f32_e32 v33, v48, v35
	s_and_b64 vcc, exec, s[28:29]
	v_cvt_pk_fp8_f32 v49, v32, v33 op_sel:[0,0,1]
	v_mov_b32_e32 v32, 0
	v_mov_b32_e32 v33, 0
	s_nop 1
	v_mul_f32_e32 v16, v48, v16
	v_mul_f32_e32 v17, v48, v17
	v_cvt_pk_fp8_f32 v32, v16, v17
	v_mul_f32_e32 v16, v48, v36
	v_mul_f32_e32 v17, v48, v37
	v_cvt_pk_fp8_f32 v33, v16, v17
	v_mul_f32_e32 v18, v48, v18
	v_mul_f32_e32 v19, v48, v19
	v_mul_f32_e32 v16, v48, v38
	v_mul_f32_e32 v17, v48, v39
	v_cvt_pk_fp8_f32 v32, v18, v19 op_sel:[0,0,1]
	v_cvt_pk_fp8_f32 v33, v16, v17 op_sel:[0,0,1]
	v_mul_f32_e32 v16, v48, v20
	v_mul_f32_e32 v17, v48, v21
	v_mov_b32_e32 v18, 0
	v_cvt_pk_fp8_f32 v18, v16, v17
	v_mul_f32_e32 v17, v48, v22
	v_mul_f32_e32 v19, v48, v23
	v_mov_b32_e32 v22, 0
	v_cvt_pk_fp8_f32 v18, v17, v19 op_sel:[0,0,1]
	v_mul_f32_e32 v17, v48, v40
	v_mul_f32_e32 v19, v48, v41
	v_cvt_pk_fp8_f32 v22, v17, v19
	v_mul_f32_e32 v17, v48, v24
	v_mul_f32_e32 v19, v48, v25
	v_mov_b32_e32 v23, 0
	v_cvt_pk_fp8_f32 v23, v17, v19
	v_mul_f32_e32 v17, v48, v26
	v_mul_f32_e32 v19, v48, v27
	v_mov_b32_e32 v24, 0
	v_cvt_pk_fp8_f32 v23, v17, v19 op_sel:[0,0,1]
	v_mul_f32_e32 v17, v48, v44
	v_mul_f32_e32 v19, v48, v45
	v_cvt_pk_fp8_f32 v24, v17, v19
	v_mul_f32_e32 v17, v48, v28
	v_mul_f32_e32 v19, v48, v29
	v_mov_b32_e32 v25, 0
	v_cvt_pk_fp8_f32 v25, v17, v19
	v_mul_f32_e32 v20, v48, v42
	v_mul_f32_e32 v21, v48, v43
	v_cvt_pk_fp8_f32 v22, v20, v21 op_sel:[0,0,1]
	v_mul_f32_e32 v20, v48, v46
	v_mul_f32_e32 v21, v48, v47
	v_cvt_pk_fp8_f32 v24, v20, v21 op_sel:[0,0,1]
	v_mul_f32_e32 v17, v48, v30
	v_mul_f32_e32 v19, v48, v31
	v_add_u32_e32 v16, 0x10000, v196
	v_cvt_pk_fp8_f32 v25, v17, v19 op_sel:[0,0,1]
	ds_write2_b32 v16, v49, v33 offset1:2
	ds_write2_b32 v16, v32, v18 offset0:8 offset1:10
	ds_write2_b32 v16, v22, v24 offset0:4 offset1:6
	ds_write2_b32 v16, v23, v25 offset0:12 offset1:14
	v_add_u32_e32 v16, s6, v172
	v_ashrrev_i32_e32 v17, 31, v16
	s_waitcnt lgkmcnt(0)
	v_lshlrev_b64 v[16:17], 9, v[16:17]
	v_lshl_add_u64 v[20:21], s[12:13], 0, v[16:17]
	s_and_b32 s6, s4, 0x1c0
	ds_read_b128 v[16:19], v197
	v_lshl_add_u64 v[24:25], v[20:21], 0, s[6:7]
	ds_read_b128 v[20:23], v198
	v_lshl_add_u64 v[24:25], v[24:25], 0, v[170:171]
	v_lshl_add_u64 v[26:27], v[24:25], 0, v[184:185]
	s_waitcnt lgkmcnt(0)
	global_store_dwordx4 v[26:27], v[16:19], off sc1
	s_mov_b32 s4, s34
	v_mov_b32_e32 v172, v80
	v_lshl_add_u64 v[16:17], v[24:25], 0, v[186:187]
	global_store_dwordx4 v[16:17], v[20:23], off sc1
	s_waitcnt lgkmcnt(0)
	s_cbranch_vccnz .LBB3_18
